# source loads of the relocated w1 / w2 conversions issued without the nt hint (stores keep sc1 nt)
# speedup vs baseline: 1.0056x; 1.0056x over previous
.LBB0_623:
	v_mul_lo_u32 v50, v176, s69
	v_add_u32_e32 v158, s53, v50
	v_and_b32_e32 v179, -16, v175
	v_add_u32_e32 v50, v158, v179
	v_mul_u32_u24_e32 v51, 0x48, v106
	s_waitcnt lgkmcnt(0)
	s_barrier
	s_cmpk_lg_i32 s29, 0x100
	s_cbranch_scc1 .Lcv_skip_i0
	s_cmp_gt_u32 s74, 2
	s_cbranch_scc1 .Lcv_skip_i0
	s_load_dwordx2 s[60:61], s[0:1], 0x68
	s_load_dwordx2 s[62:63], s[0:1], 0xa0
	v_readfirstlane_b32 s87, v0
	s_lshr_b32 s87, s87, 6
	s_lshl_b32 s88, s2, 3
	s_add_i32 s88, s88, s87
	s_lshr_b32 s96, s75, 8
	s_lshl_b32 s96, s96, 1
	s_lshl_b32 s96, s96, 11
	s_add_i32 s96, s96, s88
	s_lshr_b32 s51, s96, 10
	s_add_i32 s32, s74, 1
	s_lshl_b32 s32, s32, 5
	s_add_i32 s51, s51, s32
	s_bfe_u32 s32, s96, 0x30007
	s_and_b32 s33, s96, 0x7f
	s_lshl_b32 s92, s51, 23
	s_lshl_b32 s93, s32, 20
	s_add_u32 s92, s92, s93
	s_lshl_b32 s93, s33, 6
	s_add_u32 s96, s92, s93
	s_and_b32 s92, s33, 63
	s_lshr_b32 s92, s92, 3
	s_lshl_b32 s92, s92, 8
	s_lshr_b32 s93, s33, 6
	s_lshl_b32 s93, s93, 7
	s_or_b32 s92, s92, s93
	s_and_b32 s93, s33, 7
	s_lshl_b32 s93, s93, 4
	s_or_b32 s92, s92, s93
	s_lshl_b32 s92, s92, 10
	s_lshl_b32 s93, s32, 7
	s_add_u32 s92, s92, s93
	s_lshl_b32 s93, s51, 21
	s_add_u32 s92, s92, s93
	s_add_u32 s92, s92, 0x1f00000
	s_waitcnt lgkmcnt(0)
	s_add_u32 s60, s60, s96
	s_addc_u32 s61, s61, 0
	s_add_u32 s62, s62, s92
	s_addc_u32 s63, s63, 0
	v_and_b32_e32 v195, 63, v0
	v_lshrrev_b32_e32 v196, 2, v195
	v_and_b32_e32 v195, 3, v195
	v_lshlrev_b32_e32 v196, 15, v196
	v_lshl_or_b32 v195, v195, 4, v196
	global_load_dwordx4 v[202:205], v195, s[60:61]
	v_add_u32_e32 v196, 0x2000, v195
	global_load_dwordx4 v[206:209], v196, s[60:61]
	v_add_u32_e32 v196, 0x4000, v195
	global_load_dwordx4 v[210:213], v196, s[60:61]
	v_add_u32_e32 v196, 0x6000, v195
	global_load_dwordx4 v[216:219], v196, s[60:61]
	v_add_u32_e32 v196, 0x80000, v195
	global_load_dwordx4 v[220:223], v196, s[60:61]
	v_add_u32_e32 v196, 0x82000, v195
	global_load_dwordx4 v[224:227], v196, s[60:61]
	v_add_u32_e32 v196, 0x84000, v195
	global_load_dwordx4 v[228:231], v196, s[60:61]
	v_add_u32_e32 v196, 0x86000, v195
	global_load_dwordx4 v[246:249], v196, s[60:61]

.Lcv_skip_f0:
	s_cmpk_lg_i32 s29, 0x100
	s_cbranch_scc1 .Lcv_skip_i1
	s_cmp_gt_u32 s74, 2
	s_cbranch_scc1 .Lcv_skip_i1
	s_load_dwordx2 s[60:61], s[0:1], 0x68
	s_load_dwordx2 s[62:63], s[0:1], 0xa0
	v_readfirstlane_b32 s87, v0
	s_lshr_b32 s87, s87, 6
	s_lshl_b32 s88, s2, 3
	s_add_i32 s88, s88, s87
	s_lshr_b32 s96, s75, 8
	s_lshl_b32 s96, s96, 1
	s_add_i32 s96, s96, 1
	s_lshl_b32 s96, s96, 11
	s_add_i32 s96, s96, s88
	s_lshr_b32 s51, s96, 10
	s_add_i32 s32, s74, 1
	s_lshl_b32 s32, s32, 5
	s_add_i32 s51, s51, s32
	s_bfe_u32 s32, s96, 0x30007
	s_and_b32 s33, s96, 0x7f
	s_lshl_b32 s92, s51, 23
	s_lshl_b32 s93, s32, 20
	s_add_u32 s92, s92, s93
	s_lshl_b32 s93, s33, 6
	s_add_u32 s96, s92, s93
	s_and_b32 s92, s33, 63
	s_lshr_b32 s92, s92, 3
	s_lshl_b32 s92, s92, 8
	s_lshr_b32 s93, s33, 6
	s_lshl_b32 s93, s93, 7
	s_or_b32 s92, s92, s93
	s_and_b32 s93, s33, 7
	s_lshl_b32 s93, s93, 4
	s_or_b32 s92, s92, s93
	s_lshl_b32 s92, s92, 10
	s_lshl_b32 s93, s32, 7
	s_add_u32 s92, s92, s93
	s_lshl_b32 s93, s51, 21
	s_add_u32 s92, s92, s93
	s_add_u32 s92, s92, 0x1f00000
	s_waitcnt lgkmcnt(0)
	s_add_u32 s60, s60, s96
	s_addc_u32 s61, s61, 0
	s_add_u32 s62, s62, s92
	s_addc_u32 s63, s63, 0
	v_and_b32_e32 v195, 63, v0
	v_lshrrev_b32_e32 v196, 2, v195
	v_and_b32_e32 v195, 3, v195
	v_lshlrev_b32_e32 v196, 15, v196
	v_lshl_or_b32 v195, v195, 4, v196
	global_load_dwordx4 v[202:205], v195, s[60:61]
	v_add_u32_e32 v196, 0x2000, v195
	global_load_dwordx4 v[206:209], v196, s[60:61]
	v_add_u32_e32 v196, 0x4000, v195
	global_load_dwordx4 v[210:213], v196, s[60:61]
	v_add_u32_e32 v196, 0x6000, v195
	global_load_dwordx4 v[216:219], v196, s[60:61]
	v_add_u32_e32 v196, 0x80000, v195
	global_load_dwordx4 v[220:223], v196, s[60:61]
	v_add_u32_e32 v196, 0x82000, v195
	global_load_dwordx4 v[224:227], v196, s[60:61]
	v_add_u32_e32 v196, 0x84000, v195
	global_load_dwordx4 v[228:231], v196, s[60:61]
	v_add_u32_e32 v196, 0x86000, v195
	global_load_dwordx4 v[246:249], v196, s[60:61]

.LBB0_1061:
	v_mov_b32_e32 v2, v243
	s_nop 15
	s_nop 15
	s_lshl_b32 s23, s51, 8
	v_readfirstlane_b32 s21, v2
	s_ashr_i32 s25, s21, 2
	s_andn2_b32 s25, s25, 63
	s_lshr_b32 s21, s21, 1
	s_add_i32 s25, s25, s23
	s_lshl_b32 s23, s76, 7
	s_and_b32 s21, s21, 0x60
	v_and_or_b32 v6, v2, 15, s25
	s_or_b32 s21, s21, s23
	v_lshrrev_b32_e32 v2, 1, v2
	v_and_or_b32 v4, v2, 24, s21
	s_waitcnt vmcnt(8)
	s_mov_b32 s32, 0
	s_cmp_gt_u32 s74, 2
	s_cbranch_scc1 .Lcg_skip_i
	s_cmp_gt_u32 s51, 0x1ff
	s_cbranch_scc1 .Lcg_skip_i
	s_load_dword s101, s[0:1], 0xb0
	s_load_dwordx2 s[80:81], s[0:1], 0x78
	s_load_dwordx2 s[82:83], s[0:1], 0xa0
	v_readlane_b32 s84, v255, 7
	v_readfirstlane_b32 s85, v0
	s_lshr_b32 s85, s85, 6
	s_lshl_b32 s84, s84, 3
	s_add_i32 s84, s84, s85
	s_bfe_u32 s85, s51, 0x30006
	s_lshl_b32 s85, s85, 11
	s_add_i32 s85, s85, s84
	s_lshr_b32 s84, s85, 9
	s_add_i32 s92, s74, 1
	s_lshl_b32 s92, s92, 5
	s_add_i32 s84, s84, s92
	s_lshl_b32 s92, s84, 22
	s_bfe_u32 s93, s85, 0x30006
	s_lshl_b32 s93, s93, 19
	s_add_u32 s92, s92, s93
	s_and_b32 s93, s85, 63
	s_lshl_b32 s93, s93, 6
	s_add_u32 s92, s92, s93
	s_bfe_u32 s93, s51, 0x10005
	s_lshl_b32 s93, s93, 18
	s_add_u32 s100, s92, s93
	s_lshl_b32 s92, s84, 20
	s_and_b32 s93, s85, 63
	s_lshl_b32 s93, s93, 14
	s_add_u32 s92, s92, s93
	s_bfe_u32 s93, s85, 0x30006
	s_lshl_b32 s93, s93, 7
	s_add_u32 s92, s92, s93
	s_bfe_u32 s93, s51, 0x10005
	s_lshl_b32 s93, s93, 6
	s_add_u32 s92, s92, s93
	s_add_u32 s92, s92, 0x21f00000
	s_waitcnt lgkmcnt(0)
	s_cmpk_lg_i32 s101, 0x100
	s_cbranch_scc1 .Lcg_skip_i
	s_add_u32 s80, s80, s100
	s_addc_u32 s81, s81, 0
	s_add_u32 s82, s82, s92
	s_addc_u32 s83, s83, 0
	v_and_b32_e32 v56, 63, v0
	v_lshrrev_b32_e32 v57, 2, v56
	v_and_b32_e32 v56, 3, v56
	v_lshlrev_b32_e32 v57, 14, v57
	v_lshl_or_b32 v56, v56, 4, v57
	global_load_dwordx4 v[24:27], v56, s[80:81]
	v_add_u32_e32 v57, 0x1000, v56
	global_load_dwordx4 v[28:31], v57, s[80:81]
	v_add_u32_e32 v57, 0x2000, v56
	global_load_dwordx4 v[32:35], v57, s[80:81]
	v_add_u32_e32 v57, 0x3000, v56
	global_load_dwordx4 v[36:39], v57, s[80:81]
	s_mov_b32 s32, 1
